# baseline (speedup 1.0000x reference)
_Z10enc_kernelPKfS0_PK15HIP_vector_typeIjLj4EES4_S4_S0_S0_S0_Pf:
	s_load_dwordx4 s[12:15], s[0:1], 0x0
	s_load_dwordx2 s[16:17], s[0:1], 0x10
	s_load_dwordx8 s[4:11], s[0:1], 0x28
	v_lshrrev_b32_e32 v56, 6, v0
	s_lshl_b32 s2, s2, 6
	v_lshl_or_b32 v47, v56, 4, s2
	v_and_b32_e32 v57, 15, v0
	v_or_b32_e32 v2, v47, v57
	v_ashrrev_i32_e32 v3, 31, v2
	s_waitcnt lgkmcnt(0)
	v_and_b32_e32 v119, 48, v0
	global_load_dwordx4 v[120:123], v119, s[4:5]
	global_load_dwordx4 v[124:127], v119, s[4:5] offset:64
	global_load_dwordx4 v[128:131], v119, s[4:5] offset:128
	global_load_dwordx4 v[132:135], v119, s[4:5] offset:192
	global_load_dwordx4 v[136:139], v119, s[4:5] offset:256
	global_load_dwordx4 v[140:143], v119, s[4:5] offset:320
	global_load_dwordx4 v[144:147], v119, s[4:5] offset:384
	global_load_dwordx4 v[148:151], v119, s[4:5] offset:448
	global_load_dwordx4 v[192:195], v119, s[6:7]
	global_load_dwordx4 v[248:251], v119, s[6:7] offset:64
	global_load_dwordx4 v[196:199], v119, s[6:7] offset:128
	global_load_dwordx4 v[164:167], v119, s[6:7] offset:192
	global_load_dwordx4 v[224:227], v119, s[6:7] offset:256
	global_load_dwordx4 v[232:235], v119, s[6:7] offset:320
	global_load_dwordx4 v[200:203], v119, s[8:9]
	global_load_dwordx4 v[180:183], v119, s[8:9] offset:64
	global_load_dwordx4 v[204:207], v119, s[8:9] offset:128
	global_load_dwordx4 v[188:191], v119, s[8:9] offset:192
	v_lshl_add_u64 v[4:5], v[2:3], 2, s[14:15]
	global_load_dword v46, v[4:5], off
	v_mov_b32_e32 v45, 0
	v_lshlrev_b64 v[2:3], 9, v[2:3]
	v_lshlrev_b32_e32 v44, 4, v0
	v_lshl_add_u64 v[2:3], s[12:13], 0, v[2:3]
	v_and_b32_e32 v48, 48, v0
	v_mov_b32_e32 v49, v45
	v_lshl_add_u64 v[4:5], s[16:17], 0, v[44:45]
	v_lshl_add_u64 v[42:43], v[2:3], 0, v[48:49]
	s_movk_i32 s0, 0x2000
	v_add_co_u32_e32 v2, vcc, s0, v4
	s_movk_i32 s0, 0x4000
	s_nop 0
	v_addc_co_u32_e32 v3, vcc, 0, v5, vcc
	v_add_co_u32_e32 v6, vcc, s0, v4
	s_movk_i32 s0, 0x6000
	s_nop 0
	v_addc_co_u32_e32 v7, vcc, 0, v5, vcc
	global_load_dwordx4 v[18:21], v44, s[16:17]
	global_load_dwordx4 v[22:25], v[2:3], off offset:-4096
	global_load_dwordx4 v[26:29], v[2:3], off
	global_load_dwordx4 v[30:33], v[6:7], off offset:-4096
	v_add_co_u32_e32 v2, vcc, s0, v4
	s_mov_b32 s0, 0x8000
	s_nop 0
	v_addc_co_u32_e32 v3, vcc, 0, v5, vcc
	global_load_dwordx4 v[34:37], v[6:7], off
	global_load_dwordx4 v[38:41], v[2:3], off offset:-4096
	v_add_co_u32_e32 v6, vcc, s0, v4
	s_mov_b32 s0, 0xa000
	s_nop 0
	v_addc_co_u32_e32 v7, vcc, 0, v5, vcc
	global_load_dwordx4 v[50:53], v[2:3], off
	global_load_dwordx4 v[58:61], v[6:7], off offset:-4096
	v_add_co_u32_e32 v2, vcc, s0, v4
	s_mov_b32 s0, 0xc000
	s_nop 0
	v_addc_co_u32_e32 v3, vcc, 0, v5, vcc
	global_load_dwordx4 v[62:65], v[6:7], off
	global_load_dwordx4 v[66:69], v[2:3], off offset:-4096
	v_add_co_u32_e32 v6, vcc, s0, v4
	s_mov_b32 s0, 0xe000
	s_nop 0
	v_addc_co_u32_e32 v7, vcc, 0, v5, vcc
	global_load_dwordx4 v[70:73], v[2:3], off
	global_load_dwordx4 v[74:77], v[6:7], off offset:-4096
	v_add_co_u32_e32 v2, vcc, s0, v4
	s_mov_b32 s0, 0x10000
	s_nop 0
	v_addc_co_u32_e32 v3, vcc, 0, v5, vcc
	v_add_co_u32_e32 v4, vcc, s0, v4
	global_load_dwordx4 v[78:81], v[6:7], off
	global_load_dwordx4 v[82:85], v[2:3], off offset:-4096
	v_addc_co_u32_e32 v5, vcc, 0, v5, vcc
	global_load_dwordx4 v[86:89], v[2:3], off
	global_load_dwordx4 v[90:93], v[4:5], off offset:-4096
	global_load_dwordx4 v[94:97], v[4:5], off
	global_load_dwordx4 v[98:101], v[42:43], off
	global_load_dwordx4 v[102:105], v[42:43], off offset:64
	global_load_dwordx4 v[106:109], v[42:43], off offset:128
	global_load_dwordx4 v[110:113], v[42:43], off offset:192
	global_load_dwordx4 v[10:13], v[42:43], off offset:256
	global_load_dwordx4 v[14:17], v[42:43], off offset:320
	s_nop 0
	global_load_dwordx4 v[2:5], v[42:43], off offset:384
	global_load_dwordx4 v[6:9], v[42:43], off offset:448
	v_or_b32_e32 v1, 0x10000, v44
	v_and_b32_e32 v49, 63, v0
	s_movk_i32 s0, 0x1040
	s_movk_i32 s2, 0x104
	v_cmp_gt_u32_e32 vcc, 16, v49
	s_waitcnt vmcnt(24)
	ds_write_b128 v44, v[18:21]
	s_waitcnt vmcnt(23)
	ds_write_b128 v44, v[22:25] offset:4096
	s_waitcnt vmcnt(22)
	ds_write_b128 v44, v[26:29] offset:8192
	s_waitcnt vmcnt(21)
	ds_write_b128 v44, v[30:33] offset:12288
	s_waitcnt vmcnt(20)
	ds_write_b128 v44, v[34:37] offset:16384
	s_waitcnt vmcnt(19)
	ds_write_b128 v44, v[38:41] offset:20480
	s_waitcnt vmcnt(18)
	ds_write_b128 v44, v[50:53] offset:24576
	s_waitcnt vmcnt(17)
	ds_write_b128 v44, v[58:61] offset:28672
	s_waitcnt vmcnt(16)
	ds_write_b128 v44, v[62:65] offset:32768
	s_waitcnt vmcnt(15)
	ds_write_b128 v44, v[66:69] offset:36864
	s_waitcnt vmcnt(14)
	ds_write_b128 v44, v[70:73] offset:40960
	s_waitcnt vmcnt(13)
	ds_write_b128 v44, v[74:77] offset:45056
	s_waitcnt vmcnt(12)
	ds_write_b128 v44, v[78:81] offset:49152
	s_waitcnt vmcnt(11)
	ds_write_b128 v44, v[82:85] offset:53248
	s_waitcnt vmcnt(10)
	ds_write_b128 v44, v[86:89] offset:57344
	s_waitcnt vmcnt(9)
	ds_write_b128 v44, v[90:93] offset:61440
	s_waitcnt vmcnt(8)
	ds_write_b128 v1, v[94:97]
	s_waitcnt lgkmcnt(0)
	s_barrier
	s_waitcnt vmcnt(0)
	v_pk_fma_f32 v[18:19], v[98:99], -2.0, v[46:47] op_sel_hi:[1,0,0]
	v_pk_fma_f32 v[20:21], v[100:101], -2.0, v[46:47] op_sel_hi:[1,0,0]
	v_pk_fma_f32 v[22:23], v[102:103], -2.0, v[46:47] op_sel_hi:[1,0,0]
	v_pk_fma_f32 v[36:37], v[104:105], -2.0, v[46:47] op_sel_hi:[1,0,0]
	v_pk_fma_f32 v[38:39], v[106:107], -2.0, v[46:47] op_sel_hi:[1,0,0]
	v_cvt_pk_bf16_f32 v18, v18, v19
	v_cvt_pk_bf16_f32 v19, v20, v21
	v_cvt_pk_bf16_f32 v20, v22, v23
	v_cvt_pk_bf16_f32 v21, v36, v37
	v_cvt_pk_bf16_f32 v22, v38, v39
	v_lshlrev_b32_e32 v44, 4, v49
	ds_read_b128 v[58:61], v44
	ds_read_b128 v[62:65], v44 offset:1024
	ds_read_b128 v[66:69], v44 offset:4096
	ds_read_b128 v[70:73], v44 offset:5120
	ds_read_b128 v[74:77], v44 offset:8192
	ds_read_b128 v[78:81], v44 offset:9216
	ds_read_b128 v[82:85], v44 offset:12288
	ds_read_b128 v[86:89], v44 offset:13312
	v_pk_fma_f32 v[50:51], v[108:109], -2.0, v[46:47] op_sel_hi:[1,0,0]
	v_pk_fma_f32 v[52:53], v[110:111], -2.0, v[46:47] op_sel_hi:[1,0,0]
	v_pk_fma_f32 v[54:55], v[112:113], -2.0, v[46:47] op_sel_hi:[1,0,0]
	v_cvt_pk_bf16_f32 v23, v50, v51
	v_pk_fma_f32 v[0:1], v[10:11], -2.0, v[46:47] op_sel_hi:[1,0,0]
	v_pk_fma_f32 v[12:13], v[12:13], -2.0, v[46:47] op_sel_hi:[1,0,0]
	v_cvt_pk_bf16_f32 v10, v0, v1
	v_cvt_pk_bf16_f32 v11, v12, v13
	v_pk_fma_f32 v[8:9], v[8:9], -2.0, v[46:47] op_sel_hi:[1,0,0]
	v_pk_mul_f32 v[208:209], v[46:47], v[120:121] op_sel_hi:[0,1]
	v_pk_mul_f32 v[210:211], v[46:47], v[122:123] op_sel_hi:[0,1]
	v_pk_mul_f32 v[212:213], v[46:47], v[124:125] op_sel_hi:[0,1]
	v_pk_mul_f32 v[214:215], v[46:47], v[126:127] op_sel_hi:[0,1]
	v_pk_mul_f32 v[216:217], v[46:47], v[128:129] op_sel_hi:[0,1]
	v_pk_mul_f32 v[218:219], v[46:47], v[130:131] op_sel_hi:[0,1]
	v_pk_mul_f32 v[222:223], v[46:47], v[134:135] op_sel_hi:[0,1]
	v_pk_mul_f32 v[24:25], v[46:47], v[132:133] op_sel_hi:[0,1]
	v_mov_b32_e32 v221, v25
	v_mov_b32_e32 v220, v24
	v_pk_fma_f32 v[26:27], v[14:15], -2.0, v[46:47] op_sel_hi:[1,0,0]
	v_pk_fma_f32 v[28:29], v[16:17], -2.0, v[46:47] op_sel_hi:[1,0,0]
	ds_read_b128 v[14:17], v44 offset:2048
	s_waitcnt lgkmcnt(8)
	v_mfma_f32_16x16x32_bf16 v[208:211], v[58:61], v[18:21], v[208:211]
	v_cvt_pk_bf16_f32 v24, v52, v53
	v_cvt_pk_bf16_f32 v25, v54, v55
	v_cvt_pk_bf16_f32 v12, v26, v27
	s_waitcnt lgkmcnt(2)
	v_mfma_f32_16x16x32_bf16 v[220:223], v[82:85], v[18:21], v[220:223]
	v_cvt_pk_bf16_f32 v13, v28, v29
	ds_read_b128 v[26:29], v44 offset:6144
	ds_read_b128 v[40:43], v44 offset:3072
	ds_read_b128 v[50:53], v44 offset:10240
	v_mfma_f32_16x16x32_bf16 v[208:211], v[62:65], v[22:25], v[208:211]
	v_fma_f32 v34, v2, -2.0, v46
	v_fma_f32 v35, v3, -2.0, v46
	v_pk_fma_f32 v[54:55], v[6:7], -2.0, v[46:47] op_sel_hi:[1,0,0]
	v_pk_mul_f32 v[238:239], v[46:47], v[142:143] op_sel_hi:[0,1]
	s_waitcnt lgkmcnt(3)
	v_mfma_f32_16x16x32_bf16 v[208:211], v[14:17], v[10:13], v[208:211]
	ds_read_b128 v[0:3], v44 offset:7168
	ds_read_b128 v[14:17], v44 offset:14336
	v_pk_mul_f32 v[236:237], v[46:47], v[140:141] op_sel_hi:[0,1]
	v_mfma_f32_16x16x32_bf16 v[220:223], v[86:89], v[22:25], v[220:223]
	s_waitcnt lgkmcnt(0)
	v_mfma_f32_16x16x32_bf16 v[220:223], v[14:17], v[10:13], v[220:223]
	s_nop 1
	ds_read_b128 v[30:33], v44 offset:23552
	v_mfma_f32_16x16x32_bf16 v[212:215], v[66:69], v[18:21], v[212:215]
	v_mfma_f32_16x16x32_bf16 v[212:215], v[70:73], v[22:25], v[212:215]
	v_mfma_f32_16x16x32_bf16 v[212:215], v[26:29], v[10:13], v[212:215]
	v_fma_f32 v28, v4, -2.0, v46
	v_fma_f32 v29, v5, -2.0, v46
	v_cvt_pk_bf16_f32 v26, v34, v35
	v_cvt_pk_bf16_f32 v27, v28, v29
	v_cvt_pk_bf16_f32 v28, v54, v55
	v_cvt_pk_bf16_f32 v29, v8, v9
	v_mfma_f32_16x16x32_bf16 v[216:219], v[74:77], v[18:21], v[216:219]
	ds_read_b128 v[4:7], v44 offset:11264
	v_pk_mul_f32 v[228:229], v[46:47], v[136:137] op_sel_hi:[0,1]
	v_pk_mul_f32 v[230:231], v[46:47], v[138:139] op_sel_hi:[0,1]
	v_mfma_f32_16x16x32_bf16 v[212:215], v[0:3], v[26:29], v[212:215]
	s_nop 1
	v_mfma_f32_16x16x32_bf16 v[216:219], v[78:81], v[22:25], v[216:219]
	ds_read_b128 v[34:37], v44 offset:19456
	v_mfma_f32_16x16x32_bf16 v[216:219], v[50:53], v[10:13], v[216:219]
	ds_read_b128 v[50:53], v44 offset:15360
	v_pk_mul_f32 v[242:243], v[46:47], v[146:147] op_sel_hi:[0,1]
	s_waitcnt lgkmcnt(2)
	v_mfma_f32_16x16x32_bf16 v[216:219], v[4:7], v[26:29], v[216:219]
	ds_read_b128 v[4:7], v44 offset:16384
	v_pk_mul_f32 v[240:241], v[46:47], v[144:145] op_sel_hi:[0,1]
	v_mfma_f32_16x16x32_bf16 v[208:211], v[40:43], v[26:29], v[208:211]
	ds_read_b128 v[40:43], v44 offset:17408
	s_waitcnt lgkmcnt(1)
	v_mfma_f32_16x16x32_bf16 v[228:231], v[4:7], v[18:21], v[228:231]
	ds_read_b128 v[4:7], v44 offset:18432
	ds_read_b128 v[14:17], v44 offset:27648
	s_waitcnt lgkmcnt(2)
	v_mfma_f32_16x16x32_bf16 v[228:231], v[40:43], v[22:25], v[228:231]
	v_pk_mul_f32 v[246:247], v[46:47], v[150:151] op_sel_hi:[0,1]
	s_waitcnt lgkmcnt(1)
	v_mfma_f32_16x16x32_bf16 v[228:231], v[4:7], v[10:13], v[228:231]
	ds_read_b128 v[4:7], v44 offset:20480
	v_pk_mul_f32 v[244:245], v[46:47], v[148:149] op_sel_hi:[0,1]
	v_mfma_f32_16x16x32_bf16 v[228:231], v[34:37], v[26:29], v[228:231]
	ds_read_b128 v[34:37], v44 offset:21504
	s_waitcnt lgkmcnt(1)
	v_mfma_f32_16x16x32_bf16 v[236:239], v[4:7], v[18:21], v[236:239]
	ds_read_b128 v[4:7], v44 offset:22528
	ds_read_b128 v[0:3], v44 offset:30720
	s_waitcnt lgkmcnt(2)
	v_mfma_f32_16x16x32_bf16 v[236:239], v[34:37], v[22:25], v[236:239]
	s_waitcnt lgkmcnt(1)
	v_mfma_f32_16x16x32_bf16 v[236:239], v[4:7], v[10:13], v[236:239]
	ds_read_b128 v[4:7], v44 offset:24576
	v_mfma_f32_16x16x32_bf16 v[236:239], v[30:33], v[26:29], v[236:239]
	ds_read_b128 v[30:33], v44 offset:25600
	s_waitcnt lgkmcnt(1)
	v_mfma_f32_16x16x32_bf16 v[240:243], v[4:7], v[18:21], v[240:243]
	ds_read_b128 v[4:7], v44 offset:26624
	s_waitcnt lgkmcnt(1)
	v_mfma_f32_16x16x32_bf16 v[240:243], v[30:33], v[22:25], v[240:243]
	s_waitcnt lgkmcnt(0)
	v_mfma_f32_16x16x32_bf16 v[240:243], v[4:7], v[10:13], v[240:243]
	ds_read_b128 v[4:7], v44 offset:28672
	v_mfma_f32_16x16x32_bf16 v[240:243], v[14:17], v[26:29], v[240:243]
	ds_read_b128 v[14:17], v44 offset:29696
	s_waitcnt lgkmcnt(1)
	v_mfma_f32_16x16x32_bf16 v[244:247], v[4:7], v[18:21], v[244:247]
	ds_read_b128 v[4:7], v44 offset:31744
	s_nop 3
	s_waitcnt lgkmcnt(1)
	v_mfma_f32_16x16x32_bf16 v[244:247], v[14:17], v[22:25], v[244:247]
	v_cvt_pk_bf16_f32 v20, v240, v241
	v_mfma_f32_16x16x32_bf16 v[244:247], v[0:3], v[10:13], v[244:247]
	v_cvt_pk_bf16_f32 v0, v208, v209
	v_mfma_f32_16x16x32_bf16 v[220:223], v[50:53], v[26:29], v[220:223]
	v_cvt_pk_bf16_f32 v1, v210, v211
	s_waitcnt lgkmcnt(0)
	v_mfma_f32_16x16x32_bf16 v[244:247], v[4:7], v[26:29], v[244:247]
	v_cvt_pk_bf16_f32 v2, v212, v213
	v_cvt_pk_bf16_f32 v3, v214, v215
	v_cvt_pk_bf16_f32 v4, v216, v217
	v_cvt_pk_bf16_f32 v5, v218, v219
	s_nop 0
	v_cvt_pk_bf16_f32 v6, v220, v221
	v_cvt_pk_bf16_f32 v7, v222, v223
	ds_read_b128 v[12:15], v44 offset:32768
	v_cvt_pk_bf16_f32 v8, v228, v229
	v_cvt_pk_bf16_f32 v9, v230, v231
	v_cvt_pk_bf16_f32 v10, v236, v237
	v_cvt_pk_bf16_f32 v11, v238, v239
	ds_read_b128 v[16:19], v44 offset:33792
	ds_read_b128 v[24:27], v44 offset:34816
	s_waitcnt lgkmcnt(2)
	v_mfma_f32_16x16x32_bf16 v[192:195], v[12:15], v[0:3], v[192:195]
	v_cvt_pk_bf16_f32 v21, v242, v243
	ds_read_b128 v[12:15], v44 offset:35840
	s_waitcnt lgkmcnt(2)
	v_mfma_f32_16x16x32_bf16 v[192:195], v[16:19], v[4:7], v[192:195]
	v_cvt_pk_bf16_f32 v22, v244, v245
	s_waitcnt lgkmcnt(1)
	v_mfma_f32_16x16x32_bf16 v[192:195], v[24:27], v[8:11], v[192:195]
	v_cvt_pk_bf16_f32 v23, v246, v247
	s_waitcnt lgkmcnt(0)
	s_nop 0
	v_mfma_f32_16x16x32_bf16 v[192:195], v[12:15], v[20:23], v[192:195]
	s_nop 7
	v_mul_f32_e32 v12, 0x4038aa3b, v192
	v_exp_f32_e32 v16, v12
	v_mul_f32_e32 v12, 0x4038aa3b, v193
	v_exp_f32_e32 v17, v12
	ds_read_b128 v[12:15], v44 offset:36864
	v_add_f32_e32 v16, 1.0, v16
	v_rcp_f32_e32 v28, v16
	v_add_f32_e32 v24, 1.0, v17
	ds_read_b128 v[16:19], v44 offset:37888
	v_rcp_f32_e32 v29, v24
	ds_read_b128 v[24:27], v44 offset:38912
	s_waitcnt lgkmcnt(2)
	v_mfma_f32_16x16x32_bf16 v[216:219], v[12:15], v[0:3], v[248:251]
	v_mul_f32_e32 v12, 0x4038aa3b, v194
	v_exp_f32_e32 v30, v12
	ds_read_b128 v[12:15], v44 offset:39936
	s_waitcnt lgkmcnt(2)
	v_mfma_f32_16x16x32_bf16 v[216:219], v[16:19], v[4:7], v[216:219]
	v_mul_f32_e32 v16, 0x4038aa3b, v195
	v_exp_f32_e32 v17, v16
	s_waitcnt lgkmcnt(1)
	v_mfma_f32_16x16x32_bf16 v[192:195], v[24:27], v[8:11], v[216:219]
	v_add_f32_e32 v16, 1.0, v30
	v_rcp_f32_e32 v16, v16
	v_add_f32_e32 v17, 1.0, v17
	s_waitcnt lgkmcnt(0)
	v_mfma_f32_16x16x32_bf16 v[192:195], v[12:15], v[20:23], v[192:195]
	v_rcp_f32_e32 v17, v17
	v_pk_fma_f32 v[28:29], v[28:29], -2.0, 1.0 op_sel_hi:[1,0,0]
	v_pk_fma_f32 v[30:31], v[16:17], -2.0, 1.0 op_sel_hi:[1,0,0]
	s_nop 4
	v_mul_f32_e32 v12, 0x4038aa3b, v192
	v_exp_f32_e32 v12, v12
	v_mul_f32_e32 v13, 0x4038aa3b, v193
	v_exp_f32_e32 v13, v13
	v_mov_b32_e32 v35, v195
	v_add_f32_e32 v12, 1.0, v12
	v_rcp_f32_e32 v24, v12
	v_add_f32_e32 v18, 1.0, v13
	ds_read_b128 v[12:15], v44 offset:40960
	v_rcp_f32_e32 v25, v18
	ds_read_b128 v[16:19], v44 offset:41984
	s_waitcnt lgkmcnt(1)
	v_mfma_f32_16x16x32_bf16 v[196:199], v[12:15], v[0:3], v[196:199]
	v_fma_f32 v32, v24, -2.0, 1.0
	v_fma_f32 v33, v25, -2.0, 1.0
	v_mul_f32_e32 v34, 0x4038aa3b, v194
	ds_read_b128 v[24:27], v44 offset:43008
	ds_read_b128 v[12:15], v44 offset:44032
	s_waitcnt lgkmcnt(2)
	v_mfma_f32_16x16x32_bf16 v[192:195], v[16:19], v[4:7], v[196:199]
	v_mul_f32_e32 v16, 0x4038aa3b, v35
	v_exp_f32_e32 v16, v16
	v_exp_f32_e32 v34, v34
	s_waitcnt lgkmcnt(1)
	v_mfma_f32_16x16x32_bf16 v[192:195], v[24:27], v[8:11], v[192:195]
	v_add_f32_e32 v16, 1.0, v16
	v_rcp_f32_e32 v35, v16
	v_add_f32_e32 v17, 1.0, v34
	s_waitcnt lgkmcnt(0)
	v_mfma_f32_16x16x32_bf16 v[192:195], v[12:15], v[20:23], v[192:195]
	v_rcp_f32_e32 v34, v17
	s_nop 0
	v_pk_fma_f32 v[34:35], v[34:35], -2.0, 1.0 op_sel_hi:[1,0,0]
	s_nop 4
	s_nop 0
	v_mul_f32_e32 v12, 0x4038aa3b, v192
	v_exp_f32_e32 v16, v12
	v_mul_f32_e32 v12, 0x4038aa3b, v193
	v_exp_f32_e32 v17, v12
	ds_read_b128 v[12:15], v44 offset:45056
	v_add_f32_e32 v16, 1.0, v16
	v_rcp_f32_e32 v36, v16
	v_add_f32_e32 v24, 1.0, v17
	ds_read_b128 v[16:19], v44 offset:46080
	v_rcp_f32_e32 v37, v24
	ds_read_b128 v[24:27], v44 offset:47104
	s_waitcnt lgkmcnt(2)
	v_mfma_f32_16x16x32_bf16 v[208:211], v[12:15], v[0:3], v[164:167]
	v_mul_f32_e32 v12, 0x4038aa3b, v194
	v_exp_f32_e32 v38, v12
	ds_read_b128 v[12:15], v44 offset:48128
	s_waitcnt lgkmcnt(2)
	v_mfma_f32_16x16x32_bf16 v[208:211], v[16:19], v[4:7], v[208:211]
	v_mul_f32_e32 v17, 0x4038aa3b, v195
	v_exp_f32_e32 v17, v17
	s_waitcnt lgkmcnt(1)
	v_mfma_f32_16x16x32_bf16 v[208:211], v[24:27], v[8:11], v[208:211]
	v_add_f32_e32 v16, 1.0, v38
	v_rcp_f32_e32 v38, v16
	v_pk_fma_f32 v[36:37], v[36:37], -2.0, 1.0 op_sel_hi:[1,0,0]
	s_waitcnt lgkmcnt(0)
	v_mfma_f32_16x16x32_bf16 v[192:195], v[12:15], v[20:23], v[208:211]
	v_add_f32_e32 v13, 1.0, v17
	v_rcp_f32_e32 v39, v13
	s_nop 0
	v_pk_fma_f32 v[38:39], v[38:39], -2.0, 1.0 op_sel_hi:[1,0,0]
	s_nop 3
	v_mul_f32_e32 v12, 0x4038aa3b, v192
	v_exp_f32_e32 v12, v12
	v_mul_f32_e32 v17, 0x4038aa3b, v194
	v_exp_f32_e32 v24, v17
	v_add_f32_e32 v12, 1.0, v12
	v_rcp_f32_e32 v40, v12
	v_mul_f32_e32 v12, 0x4038aa3b, v193
	v_exp_f32_e32 v16, v12
	ds_read_b128 v[12:15], v44 offset:49152
	v_add_f32_e32 v42, 1.0, v24
	v_mov_b32_e32 v43, v195
	v_add_f32_e32 v25, 1.0, v16
	ds_read_b128 v[16:19], v44 offset:50176
	v_rcp_f32_e32 v41, v25
	ds_read_b128 v[24:27], v44 offset:51200
	s_waitcnt lgkmcnt(2)
	v_mfma_f32_16x16x32_bf16 v[192:195], v[12:15], v[0:3], v[224:227]
	v_mul_f32_e32 v12, 0x4038aa3b, v43
	v_exp_f32_e32 v43, v12
	ds_read_b128 v[12:15], v44 offset:52224
	s_waitcnt lgkmcnt(2)
	v_mfma_f32_16x16x32_bf16 v[192:195], v[16:19], v[4:7], v[192:195]
	v_rcp_f32_e32 v16, v42
	v_add_f32_e32 v17, 1.0, v43
	v_rcp_f32_e32 v17, v17
	s_waitcnt lgkmcnt(1)
	v_mfma_f32_16x16x32_bf16 v[192:195], v[24:27], v[8:11], v[192:195]
	v_fma_f32 v40, v40, -2.0, 1.0
	v_fma_f32 v41, v41, -2.0, 1.0
	v_pk_fma_f32 v[42:43], v[16:17], -2.0, 1.0 op_sel_hi:[1,0,0]
	s_waitcnt lgkmcnt(0)
	v_mfma_f32_16x16x32_bf16 v[192:195], v[12:15], v[20:23], v[192:195]
	s_nop 7
	v_mul_f32_e32 v12, 0x4038aa3b, v192
	v_exp_f32_e32 v16, v12
	v_mul_f32_e32 v17, 0x4038aa3b, v193
	ds_read_b128 v[12:15], v44 offset:53248
	v_exp_f32_e32 v24, v17
	v_add_f32_e32 v16, 1.0, v16
	v_rcp_f32_e32 v50, v16
	ds_read_b128 v[16:19], v44 offset:54272
	v_add_f32_e32 v24, 1.0, v24
	v_rcp_f32_e32 v51, v24
	ds_read_b128 v[24:27], v44 offset:55296
	s_waitcnt lgkmcnt(2)
	v_mfma_f32_16x16x32_bf16 v[208:211], v[12:15], v[0:3], v[232:235]
	v_mov_b32_e32 v52, v194
	v_mul_f32_e32 v0, 0x4038aa3b, v52
	v_exp_f32_e32 v12, v0
	ds_read_b128 v[0:3], v44 offset:56320
	s_waitcnt lgkmcnt(2)
	v_mfma_f32_16x16x32_bf16 v[208:211], v[16:19], v[4:7], v[208:211]
	v_mul_f32_e32 v4, 0x4038aa3b, v195
	v_exp_f32_e32 v5, v4
	s_waitcnt lgkmcnt(1)
	v_mfma_f32_16x16x32_bf16 v[192:195], v[24:27], v[8:11], v[208:211]
	v_add_f32_e32 v4, 1.0, v12
	ds_read_b128 v[10:13], v44 offset:57344
	v_add_f32_e32 v5, 1.0, v5
	s_waitcnt lgkmcnt(1)
	v_mfma_f32_16x16x32_bf16 v[192:195], v[0:3], v[20:23], v[192:195]
	v_rcp_f32_e32 v4, v4
	v_rcp_f32_e32 v5, v5
	ds_read_b128 v[18:21], v44 offset:58368
	v_pk_fma_f32 v[14:15], v[50:51], -2.0, 1.0 op_sel_hi:[1,0,0]
	v_cvt_pk_bf16_f32 v6, v36, v37
	v_pk_fma_f32 v[16:17], v[4:5], -2.0, 1.0 op_sel_hi:[1,0,0]
	v_cvt_pk_bf16_f32 v4, v32, v33
	v_cvt_pk_bf16_f32 v5, v34, v35
	v_mul_f32_e32 v2, 0x4038aa3b, v194
	v_mul_f32_e32 v3, 0x4038aa3b, v195
	v_exp_f32_e32 v2, v2
	v_exp_f32_e32 v3, v3
	v_add_f32_e32 v2, 1.0, v2
	v_add_f32_e32 v3, 1.0, v3
	v_rcp_f32_e32 v2, v2
	v_rcp_f32_e32 v3, v3
	v_mul_f32_e32 v0, 0x4038aa3b, v192
	v_mul_f32_e32 v1, 0x4038aa3b, v193
	v_exp_f32_e32 v0, v0
	v_exp_f32_e32 v1, v1
	v_pk_fma_f32 v[22:23], v[2:3], -2.0, 1.0 op_sel_hi:[1,0,0]
	v_cvt_pk_bf16_f32 v2, v28, v29
	v_cvt_pk_bf16_f32 v3, v30, v31
	v_cvt_pk_bf16_f32 v14, v14, v15
	v_cvt_pk_bf16_f32 v15, v16, v17
	v_cvt_pk_bf16_f32 v17, v22, v23
	ds_read_b128 v[22:25], v44 offset:59392
	s_waitcnt lgkmcnt(2)
	v_mfma_f32_16x16x32_bf16 v[192:195], v[10:13], v[2:5], v[200:203]
	ds_read_b128 v[10:13], v44 offset:60416
	v_add_f32_e32 v0, 1.0, v0
	v_add_f32_e32 v1, 1.0, v1
	v_rcp_f32_e32 v0, v0
	v_rcp_f32_e32 v1, v1
	v_cvt_pk_bf16_f32 v7, v38, v39
	v_cvt_pk_bf16_f32 v8, v40, v41
	v_cvt_pk_bf16_f32 v9, v42, v43
	v_pk_fma_f32 v[0:1], v[0:1], -2.0, 1.0 op_sel_hi:[1,0,0]
	s_waitcnt lgkmcnt(0)
	v_mfma_f32_16x16x32_bf16 v[200:203], v[10:13], v[2:5], v[180:183]
	v_cvt_pk_bf16_f32 v16, v0, v1
	v_mov_b32_e32 v0, 0x11000
	v_mad_u32_u24 v0, v56, s0, v0
	v_mfma_f32_16x16x32_bf16 v[192:195], v[18:21], v[6:9], v[192:195]
	ds_read_b128 v[18:21], v44 offset:61440
	v_mad_u32_u24 v1, v57, s2, v0
	v_add_u32_e32 v26, v1, v48
	v_mfma_f32_16x16x32_bf16 v[192:195], v[22:25], v[14:17], v[192:195]
	ds_read_b128 v[22:25], v44 offset:62464
	s_waitcnt lgkmcnt(1)
	v_mfma_f32_16x16x32_bf16 v[200:203], v[18:21], v[6:9], v[200:203]
	ds_read_b128 v[18:21], v44 offset:64512
	s_nop 3
	ds_write2_b32 v26, v192, v193 offset0:1 offset1:2
	ds_write2_b32 v26, v194, v195 offset0:3 offset1:4
	ds_read_b128 v[10:13], v44 offset:63488
	s_waitcnt lgkmcnt(4)
	v_mfma_f32_16x16x32_bf16 v[192:195], v[22:25], v[14:17], v[200:203]
	s_nop 7
	ds_write2_b32 v26, v192, v193 offset0:17 offset1:18
	v_or_b32_e32 v22, 0x10000, v44
	ds_read_b128 v[22:25], v22
	s_waitcnt lgkmcnt(2)
	v_mfma_f32_16x16x32_bf16 v[200:203], v[10:13], v[2:5], v[204:207]
	v_or_b32_e32 v10, 0x10400, v44
	ds_read_b128 v[10:13], v10
	v_mov_b32_e32 v27, v195
	v_mfma_f32_16x16x32_bf16 v[200:203], v[18:21], v[6:9], v[200:203]
	v_or_b32_e32 v18, 0x10800, v44
	ds_read_b128 v[18:21], v18
	v_mov_b32_e32 v28, v194
	s_waitcnt lgkmcnt(2)
	v_mfma_f32_16x16x32_bf16 v[192:195], v[22:25], v[14:17], v[200:203]
	v_or_b32_e32 v22, 0x10c00, v44
	ds_read_b128 v[22:25], v22
	ds_write2_b32 v26, v28, v27 offset0:19 offset1:20
	s_waitcnt lgkmcnt(3)
	v_mfma_f32_16x16x32_bf16 v[196:199], v[10:13], v[2:5], v[188:191]
	s_waitcnt lgkmcnt(2)
	v_mfma_f32_16x16x32_bf16 v[196:199], v[18:21], v[6:9], v[196:199]
	s_nop 0
	ds_write2_b32 v26, v192, v193 offset0:33 offset1:34
	v_mov_b32_e32 v2, v195
	v_mov_b32_e32 v3, v194
	s_waitcnt lgkmcnt(2)
	v_mfma_f32_16x16x32_bf16 v[192:195], v[22:25], v[14:17], v[196:199]
	ds_write2_b32 v26, v3, v2 offset0:35 offset1:36
	s_nop 6
	ds_write2_b32 v26, v192, v193 offset0:49 offset1:50
	v_mov_b32_e32 v2, v195
	v_mov_b32_e32 v3, v194
	ds_write2_b32 v26, v3, v2 offset0:51 offset1:52
	s_and_saveexec_b64 s[0:1], vcc
	ds_write_b32 v1, v46
	s_or_b64 exec, exec, s[0:1]
	v_add_u32_e32 v2, v0, v44
	v_mov_b64_e32 v[0:1], s[10:11]
	v_mad_u64_u32 v[0:1], s[0:1], v47, s2, v[0:1]
	ds_read_b128 v[4:7], v2
	v_lshl_add_u64 v[8:9], v[0:1], 0, v[44:45]
	s_waitcnt lgkmcnt(0)
	global_store_dwordx4 v[8:9], v[4:7], off sc1
	s_nop 1
	s_mov_b64 s[0:1], 0x400
	ds_read_b128 v[4:7], v2 offset:1024
	v_lshl_add_u64 v[10:11], v[8:9], 0, s[0:1]
	s_waitcnt lgkmcnt(0)
	global_store_dwordx4 v[10:11], v[4:7], off sc1
	s_nop 1
	s_mov_b64 s[0:1], 0x800
	ds_read_b128 v[4:7], v2 offset:2048
	v_lshl_add_u64 v[10:11], v[8:9], 0, s[0:1]
	s_waitcnt lgkmcnt(0)
	global_store_dwordx4 v[10:11], v[4:7], off sc1
	s_nop 1
	s_mov_b64 s[0:1], 0xc00
	ds_read_b128 v[4:7], v2 offset:3072
	v_lshl_add_u64 v[8:9], v[8:9], 0, s[0:1]
	s_waitcnt lgkmcnt(0)
	global_store_dwordx4 v[8:9], v[4:7], off sc1
	s_nop 1
	v_or_b32_e32 v3, 0x100, v49
	v_cmp_gt_u32_e32 vcc, s2, v3
	s_and_saveexec_b64 s[0:1], vcc
	s_cbranch_execz .LBB2_4
	ds_read_b128 v[4:7], v2 offset:4096
	v_lshlrev_b32_e32 v2, 4, v3
	v_mov_b32_e32 v3, 0
	v_lshl_add_u64 v[0:1], v[0:1], 0, v[2:3]
	s_waitcnt lgkmcnt(0)
	global_store_dwordx4 v[0:1], v[4:7], off sc1
	s_nop 1

	.amdhsa_kernel _Z10enc_kernelPKfS0_PK15HIP_vector_typeIjLj4EES4_S4_S0_S0_S0_Pf
		.amdhsa_group_segment_fixed_size 86272
		.amdhsa_private_segment_fixed_size 0
		.amdhsa_kernarg_size 72
		.amdhsa_user_sgpr_count 2
		.amdhsa_user_sgpr_dispatch_ptr 0
		.amdhsa_user_sgpr_queue_ptr 0
		.amdhsa_user_sgpr_kernarg_segment_ptr 1
		.amdhsa_user_sgpr_dispatch_id 0
		.amdhsa_user_sgpr_kernarg_preload_length 0
		.amdhsa_user_sgpr_kernarg_preload_offset 0
		.amdhsa_user_sgpr_private_segment_size 0
		.amdhsa_uses_dynamic_stack 0
		.amdhsa_enable_private_segment 0
		.amdhsa_system_sgpr_workgroup_id_x 1
		.amdhsa_system_sgpr_workgroup_id_y 0
		.amdhsa_system_sgpr_workgroup_id_z 0
		.amdhsa_system_sgpr_workgroup_info 0
		.amdhsa_system_vgpr_workitem_id 0
		.amdhsa_next_free_vgpr 257
		.amdhsa_next_free_sgpr 96
		.amdhsa_accum_offset 252
		.amdhsa_reserve_vcc 1
		.amdhsa_float_round_mode_32 0
		.amdhsa_float_round_mode_16_64 0
		.amdhsa_float_denorm_mode_32 3
		.amdhsa_float_denorm_mode_16_64 3
		.amdhsa_dx10_clamp 1
		.amdhsa_ieee_mode 1
		.amdhsa_fp16_overflow 0
		.amdhsa_tg_split 0
		.amdhsa_exception_fp_ieee_invalid_op 0
		.amdhsa_exception_fp_denorm_src 0
		.amdhsa_exception_fp_ieee_div_zero 0
		.amdhsa_exception_fp_ieee_overflow 0
		.amdhsa_exception_fp_ieee_underflow 0
		.amdhsa_exception_fp_ieee_inexact 0
		.amdhsa_exception_int_div_zero 0
	.end_amdhsa_kernel

amdhsa.kernels:
  - .agpr_count:     0
    .args:
      - .actual_access:  read_only
        .address_space:  global
        .offset:         0
        .size:           8
        .value_kind:     global_buffer
      - .actual_access:  read_only
        .address_space:  global
        .offset:         8
        .size:           8
        .value_kind:     global_buffer
      - .actual_access:  read_only
        .address_space:  global
        .offset:         16
        .size:           8
        .value_kind:     global_buffer
      - .actual_access:  read_only
        .address_space:  global
        .offset:         24
        .size:           8
        .value_kind:     global_buffer
      - .actual_access:  read_only
        .address_space:  global
        .offset:         32
        .size:           8
        .value_kind:     global_buffer
      - .actual_access:  read_only
        .address_space:  global
        .offset:         40
        .size:           8
        .value_kind:     global_buffer
      - .actual_access:  read_only
        .address_space:  global
        .offset:         48
        .size:           8
        .value_kind:     global_buffer
      - .actual_access:  read_only
        .address_space:  global
        .offset:         56
        .size:           8
        .value_kind:     global_buffer
      - .address_space:  global
        .offset:         64
        .size:           8
        .value_kind:     global_buffer
      - .offset:         72
        .size:           4
        .value_kind:     hidden_block_count_x
      - .offset:         76
        .size:           4
        .value_kind:     hidden_block_count_y
      - .offset:         80
        .size:           4
        .value_kind:     hidden_block_count_z
      - .offset:         84
        .size:           2
        .value_kind:     hidden_group_size_x
      - .offset:         86
        .size:           2
        .value_kind:     hidden_group_size_y
      - .offset:         88
        .size:           2
        .value_kind:     hidden_group_size_z
      - .offset:         90
        .size:           2
        .value_kind:     hidden_remainder_x
      - .offset:         92
        .size:           2
        .value_kind:     hidden_remainder_y
      - .offset:         94
        .size:           2
        .value_kind:     hidden_remainder_z
      - .offset:         112
        .size:           8
        .value_kind:     hidden_global_offset_x
      - .offset:         120
        .size:           8
        .value_kind:     hidden_global_offset_y
      - .offset:         128
        .size:           8
        .value_kind:     hidden_global_offset_z
      - .offset:         136
        .size:           2
        .value_kind:     hidden_grid_dims
    .group_segment_fixed_size: 256
    .kernarg_segment_align: 8
    .kernarg_segment_size: 328
    .language:       OpenCL C
    .language_version:
      - 2
      - 0
    .max_flat_workgroup_size: 256
    .name:           _Z11prep_kernelPKfS0_S0_S0_S0_S0_S0_PKiPc
    .private_segment_fixed_size: 0
    .sgpr_count:     58
    .sgpr_spill_count: 0
    .symbol:         _Z11prep_kernelPKfS0_S0_S0_S0_S0_S0_PKiPc.kd
    .uniform_work_group_size: 1
    .uses_dynamic_stack: false
    .vgpr_count:     37
    .vgpr_spill_count: 0
    .wavefront_size: 64
  - .agpr_count:     0
    .args:
      - .actual_access:  read_only
        .address_space:  global
        .offset:         0
        .size:           8
        .value_kind:     global_buffer
      - .address_space:  global
        .offset:         8
        .size:           8
        .value_kind:     global_buffer
      - .actual_access:  read_only
        .address_space:  global
        .offset:         16
        .size:           8
        .value_kind:     global_buffer
      - .actual_access:  read_only
        .address_space:  global
        .offset:         24
        .size:           8
        .value_kind:     global_buffer
      - .address_space:  global
        .offset:         32
        .size:           8
        .value_kind:     global_buffer
      - .address_space:  global
        .offset:         40
        .size:           8
        .value_kind:     global_buffer
      - .actual_access:  read_only
        .address_space:  global
        .offset:         48
        .size:           8
        .value_kind:     global_buffer
      - .offset:         56
        .size:           4
        .value_kind:     by_value
      - .offset:         64
        .size:           4
        .value_kind:     hidden_block_count_x
      - .offset:         68
        .size:           4
        .value_kind:     hidden_block_count_y
      - .offset:         72
        .size:           4
        .value_kind:     hidden_block_count_z
      - .offset:         76
        .size:           2
        .value_kind:     hidden_group_size_x
      - .offset:         78
        .size:           2
        .value_kind:     hidden_group_size_y
      - .offset:         80
        .size:           2
        .value_kind:     hidden_group_size_z
      - .offset:         82
        .size:           2
        .value_kind:     hidden_remainder_x
      - .offset:         84
        .size:           2
        .value_kind:     hidden_remainder_y
      - .offset:         86
        .size:           2
        .value_kind:     hidden_remainder_z
      - .offset:         104
        .size:           8
        .value_kind:     hidden_global_offset_x
      - .offset:         112
        .size:           8
        .value_kind:     hidden_global_offset_y
      - .offset:         120
        .size:           8
        .value_kind:     hidden_global_offset_z
      - .offset:         128
        .size:           2
        .value_kind:     hidden_grid_dims
    .group_segment_fixed_size: 135936
    .kernarg_segment_align: 8
    .kernarg_segment_size: 320
    .language:       OpenCL C
    .language_version:
      - 2
      - 0
    .max_flat_workgroup_size: 768
    .name:           _Z11main_kernelPKfPKiPK15HIP_vector_typeIjLj4EES0_PfS7_S2_i
    .private_segment_fixed_size: 0
    .sgpr_count:     66
    .sgpr_spill_count: 0
    .symbol:         _Z11main_kernelPKfPKiPK15HIP_vector_typeIjLj4EES0_PfS7_S2_i.kd
    .uniform_work_group_size: 1
    .uses_dynamic_stack: false
    .vgpr_count:     168
    .vgpr_spill_count: 0
    .wavefront_size: 64
  - .agpr_count:     0
    .args:
      - .actual_access:  read_only
        .address_space:  global
        .offset:         0
        .size:           8
        .value_kind:     global_buffer
      - .actual_access:  read_only
        .address_space:  global
        .offset:         8
        .size:           8
        .value_kind:     global_buffer
      - .actual_access:  read_only
        .address_space:  global
        .offset:         16
        .size:           8
        .value_kind:     global_buffer
      - .actual_access:  read_only
        .address_space:  global
        .offset:         24
        .size:           8
        .value_kind:     global_buffer
      - .actual_access:  read_only
        .address_space:  global
        .offset:         32
        .size:           8
        .value_kind:     global_buffer
      - .actual_access:  read_only
        .address_space:  global
        .offset:         40
        .size:           8
        .value_kind:     global_buffer
      - .actual_access:  read_only
        .address_space:  global
        .offset:         48
        .size:           8
        .value_kind:     global_buffer
      - .actual_access:  read_only
        .address_space:  global
        .offset:         56
        .size:           8
        .value_kind:     global_buffer
      - .address_space:  global
        .offset:         64
        .size:           8
        .value_kind:     global_buffer
    .group_segment_fixed_size: 86272
    .kernarg_segment_align: 8
    .kernarg_segment_size: 72
    .language:       OpenCL C
    .language_version:
      - 2
      - 0
    .max_flat_workgroup_size: 256
    .name:           _Z10enc_kernelPKfS0_PK15HIP_vector_typeIjLj4EES4_S4_S0_S0_S0_Pf
    .private_segment_fixed_size: 0
    .sgpr_count:     24
    .sgpr_spill_count: 0
    .symbol:         _Z10enc_kernelPKfS0_PK15HIP_vector_typeIjLj4EES4_S4_S0_S0_S0_Pf.kd
    .uniform_work_group_size: 1
    .uses_dynamic_stack: false
    .vgpr_count:     252
    .vgpr_spill_count: 0
    .wavefront_size: 64
